# mLSTM item prologues (both passes): each gate pair (input/forget pre-activations of a token) fetched with one round trip instead of two
# speedup vs baseline: 1.0045x; 1.0045x over previous
; DI float softcap(float x) { return 15.0f * tanhf(x * (1.0f / 15.0f)); }
; DI float logsigmoid(float y) { return fminf(y, 0.f) - log1pf(__expf(-fabsf(y))); }
; DI void mlstm_pass1(const Params& P, LAS unsigned char* lds, int st, int g) {
;     ...
;     if (wid < nchunks) { const int t0c = chunk_tok0(wid);
;         const int p0 = dir ? 127 - 2 * lane : 2 * lane, p1 = dir ? 126 - 2 * lane : 2 * lane + 1;
;         const float* g0 = gates + (size_t)(t0c + p0) * 16; const float* g1 = gates + (size_t)(t0c + p1) * 16;
;         const float li0 = softcap(g0[dir * 8 + h]), li1 = softcap(g1[dir * 8 + h]); const float lf0 = logsigmoid(softcap(g0[dir * 8 + 4 + h])), lf1 = logsigmoid(softcap(g1[dir * 8 + 4 + h]));
.LBB0_445:
	v_and_b32_e32 v5, 63, v4
	v_lshlrev_b32_e32 v2, 1, v5
	s_lshl_b32 s2, s5, 7
	v_xor_b32_e32 v0, 0x7f, v2
	s_add_i32 s6, s4, s2
	v_cndmask_b32_e64 v6, v0, v2, s[0:1]
	v_add_u32_e32 v0, s6, v6
	v_ashrrev_i32_e32 v1, 31, v0
	v_lshlrev_b64 v[0:1], 6, v[0:1]
	s_and_b32 s2, s38, -5
	v_lshl_add_u64 v[0:1], s[22:23], 0, v[0:1]
	s_ashr_i32 s3, s2, 31
	v_lshl_add_u64 v[0:1], s[2:3], 2, v[0:1]
	global_load_dword v3, v[0:1], off
	global_load_dword v15, v[0:1], off offset:16
	s_waitcnt vmcnt(0)
	v_mul_f32_e32 v7, 0x3d888889, v3
	v_cmp_nlt_f32_e64 s[4:5], |v7|, s49
	s_and_saveexec_b64 s[8:9], s[4:5]
	s_xor_b64 s[4:5], exec, s[8:9]
	s_cbranch_execz .LBB0_447
	v_add_f32_e64 v3, |v7|, |v7|
	v_mul_f32_e32 v8, 0x3fb8aa3b, v3
	v_rndne_f32_e32 v9, v8
	v_sub_f32_e32 v10, v8, v9
	v_fma_f32 v8, v3, s50, -v8
	v_fmac_f32_e32 v8, 0x32a5705f, v3
	v_add_f32_e32 v8, v10, v8
	v_cvt_i32_f32_e32 v9, v9
	v_exp_f32_e32 v8, v8
	v_cmp_ngt_f32_e32 vcc, s51, v3
	v_ldexp_f32 v8, v8, v9
	s_nop 0
	v_cndmask_b32_e32 v8, 0, v8, vcc
	v_cmp_nlt_f32_e32 vcc, s52, v3
	s_nop 1
	v_cndmask_b32_e32 v3, v149, v8, vcc
	v_add_f32_e32 v3, 1.0, v3
	v_rcp_f32_e32 v3, v3
	s_nop 0
	v_fma_f32 v9, v3, -2.0, 1.0
.LBB0_447:
	s_andn2_saveexec_b64 s[4:5], s[4:5]
	v_mul_f32_e32 v3, v7, v7
	v_fmamk_f32 v8, v3, 0xbbbac73d, v147
	v_fmaak_f32 v8, v3, v8, 0xbd5c1c4e
	v_fmaak_f32 v8, v3, v8, 0x3e088382
	v_fmaak_f32 v8, v3, v8, 0xbeaaaa99
	v_mul_f32_e64 v8, |v7|, v8
	v_fma_f32 v9, v3, v8, |v7|
	s_or_b64 exec, exec, s[4:5]
	v_sub_u32_e32 v3, 0x7e, v2
	v_or_b32_e32 v2, 1, v2
	v_cndmask_b32_e64 v8, v3, v2, s[0:1]
	v_add_u32_e32 v2, s6, v8
	v_ashrrev_i32_e32 v3, 31, v2
	v_lshlrev_b64 v[2:3], 6, v[2:3]
	v_lshl_add_u64 v[2:3], s[22:23], 0, v[2:3]
	v_lshl_add_u64 v[2:3], s[2:3], 2, v[2:3]
	global_load_dword v10, v[2:3], off
	global_load_dword v16, v[2:3], off offset:16
	s_waitcnt vmcnt(0)
	v_mul_f32_e32 v10, 0x3d888889, v10
	v_cmp_nlt_f32_e64 s[0:1], |v10|, s49
	s_and_saveexec_b64 s[2:3], s[0:1]
	s_xor_b64 s[0:1], exec, s[2:3]
	s_cbranch_execz .LBB0_451
	v_add_f32_e64 v11, |v10|, |v10|
	v_mul_f32_e32 v12, 0x3fb8aa3b, v11
	v_rndne_f32_e32 v13, v12
	v_sub_f32_e32 v14, v12, v13
	v_fma_f32 v12, v11, s50, -v12
	v_fmac_f32_e32 v12, 0x32a5705f, v11
	v_add_f32_e32 v12, v14, v12
	v_cvt_i32_f32_e32 v13, v13
	v_exp_f32_e32 v12, v12
	v_cmp_ngt_f32_e32 vcc, s51, v11
	v_ldexp_f32 v12, v12, v13
	s_nop 0
	v_cndmask_b32_e32 v12, 0, v12, vcc
	v_cmp_nlt_f32_e32 vcc, s52, v11
	s_nop 1
	v_cndmask_b32_e32 v11, v149, v12, vcc
	v_add_f32_e32 v11, 1.0, v11
	v_rcp_f32_e32 v11, v11
	s_nop 0
	v_fma_f32 v11, v11, -2.0, 1.0
.LBB0_451:
	s_andn2_saveexec_b64 s[0:1], s[0:1]
	v_mul_f32_e32 v11, v10, v10
	v_fmamk_f32 v12, v11, 0xbbbac73d, v147
	v_fmaak_f32 v12, v11, v12, 0xbd5c1c4e
	v_fmaak_f32 v12, v11, v12, 0x3e088382
	v_fmaak_f32 v12, v11, v12, 0xbeaaaa99
	v_mul_f32_e64 v12, |v10|, v12
	v_fma_f32 v11, v11, v12, |v10|
	s_or_b64 exec, exec, s[0:1]
	v_mov_b32_e32 v0, v15
	s_waitcnt vmcnt(0)
	v_mul_f32_e32 v12, 0x3d888889, v0
	v_cmp_nlt_f32_e64 s[0:1], |v12|, s49
	s_and_saveexec_b64 s[2:3], s[0:1]
	s_xor_b64 s[0:1], exec, s[2:3]
	s_cbranch_execz .LBB0_455
	v_add_f32_e64 v0, |v12|, |v12|
	v_mul_f32_e32 v1, 0x3fb8aa3b, v0
	v_rndne_f32_e32 v13, v1
	v_sub_f32_e32 v14, v1, v13
	v_fma_f32 v1, v0, s50, -v1
	v_fmac_f32_e32 v1, 0x32a5705f, v0
	v_add_f32_e32 v1, v14, v1
	v_cvt_i32_f32_e32 v13, v13
	v_exp_f32_e32 v1, v1
	v_cmp_ngt_f32_e32 vcc, s51, v0
	v_ldexp_f32 v1, v1, v13
	s_nop 0
	v_cndmask_b32_e32 v1, 0, v1, vcc
	v_cmp_nlt_f32_e32 vcc, s52, v0
	s_nop 1
	v_cndmask_b32_e32 v0, v149, v1, vcc
	v_add_f32_e32 v0, 1.0, v0
	v_rcp_f32_e32 v0, v0
	s_nop 0
	v_fma_f32 v13, v0, -2.0, 1.0
.LBB0_455:
	s_andn2_saveexec_b64 s[0:1], s[0:1]
	v_mul_f32_e32 v0, v12, v12
	v_fmamk_f32 v1, v0, 0xbbbac73d, v147
	v_fmaak_f32 v1, v0, v1, 0xbd5c1c4e
	v_fmaak_f32 v1, v0, v1, 0x3e088382
	v_fmaak_f32 v1, v0, v1, 0xbeaaaa99
	v_mul_f32_e64 v1, |v12|, v1
	v_fma_f32 v13, v0, v1, |v12|
	s_or_b64 exec, exec, s[0:1]
	v_mov_b32_e32 v0, v16
	s_waitcnt vmcnt(0)
	v_mul_f32_e32 v0, 0x3d888889, v0
	v_cmp_nlt_f32_e64 s[0:1], |v0|, s49
	s_and_saveexec_b64 s[2:3], s[0:1]
	s_xor_b64 s[0:1], exec, s[2:3]
	s_cbranch_execz .LBB0_459
	v_add_f32_e64 v1, |v0|, |v0|
	v_mul_f32_e32 v2, 0x3fb8aa3b, v1
	v_rndne_f32_e32 v3, v2
	v_sub_f32_e32 v14, v2, v3
	v_fma_f32 v2, v1, s50, -v2
	v_fmac_f32_e32 v2, 0x32a5705f, v1
	v_add_f32_e32 v2, v14, v2
	v_cvt_i32_f32_e32 v3, v3
	v_exp_f32_e32 v2, v2
	v_cmp_ngt_f32_e32 vcc, s51, v1
	v_ldexp_f32 v2, v2, v3
	s_nop 0
	v_cndmask_b32_e32 v2, 0, v2, vcc
	v_cmp_nlt_f32_e32 vcc, s52, v1
	s_nop 1
	v_cndmask_b32_e32 v1, v149, v2, vcc
	v_add_f32_e32 v1, 1.0, v1
	v_rcp_f32_e32 v1, v1
	s_nop 0
	v_fma_f32 v1, v1, -2.0, 1.0

; DI float softcap(float x) { return 15.0f * tanhf(x * (1.0f / 15.0f)); }
; DI float logsigmoid(float y) { return fminf(y, 0.f) - log1pf(__expf(-fabsf(y))); }
; template <bool PASS2, int DIRT>
; DI void mlstm_item(const Params& P, LAS unsigned char* lds, int st, int g) {
;     ...
;     if (wid < nchunks) { const int t0c = chunk_tok0(wid);
;         const int p0 = dir ? 127 - 2 * lane : 2 * lane, p1 = dir ? 126 - 2 * lane : 2 * lane + 1;
;         const float* g0 = gates + (size_t)(t0c + p0) * 16; const float* g1 = gates + (size_t)(t0c + p1) * 16;
;         const float li0 = softcap(g0[dir * 8 + h]), li1 = softcap(g1[dir * 8 + h]); const float lf0 = logsigmoid(softcap(g0[dir * 8 + 4 + h])), lf1 = logsigmoid(softcap(g1[dir * 8 + 4 + h]));
.LBB0_714:
	s_or_b64 exec, exec, s[2:3]
	s_bfe_u32 s0, s4, 0x10002
	s_and_b32 s48, s4, 3
	s_cmp_gt_i32 s1, 7
	s_cbranch_scc1 .LBB0_734
	s_lshl_b32 s2, s0, 14
	s_lshl_b32 s3, s96, 10
	s_lshl_b32 s4, s1, 7
	v_and_b32_e32 v65, 63, v70
	s_or_b32 s2, s2, 0x3f80
	s_add_i32 s3, s3, s4
	s_sub_i32 s6, s2, s3
	v_lshlrev_b32_e32 v71, 1, v65
	v_bitop3_b32 v66, v71, s6, v200 bitop3:0xde
	v_ashrrev_i32_e32 v67, 31, v66
	v_lshlrev_b64 v[66:67], 6, v[66:67]
	v_lshl_add_u64 v[66:67], s[38:39], 0, v[66:67]
	s_lshl_b32 s40, s48, 2
	v_lshl_add_u64 v[66:67], v[66:67], 0, s[40:41]
	global_load_dword v68, v[66:67], off offset:32
	global_load_dword v244, v[66:67], off offset:48
	s_waitcnt vmcnt(0)
	v_mul_f32_e32 v72, 0x3d888889, v68
	v_cmp_nlt_f32_e64 s[2:3], |v72|, s66
	s_and_saveexec_b64 s[4:5], s[2:3]
	s_xor_b64 s[2:3], exec, s[4:5]
	s_cbranch_execz .LBB0_717
	v_add_f32_e64 v68, |v72|, |v72|
	v_mul_f32_e32 v69, 0x3fb8aa3b, v68
	v_rndne_f32_e32 v73, v69
	s_mov_b32 s4, 0x3fb8aa3b
	v_sub_f32_e32 v74, v69, v73
	v_fma_f32 v69, v68, s4, -v69
	v_fmac_f32_e32 v69, 0x32a5705f, v68
	v_add_f32_e32 v69, v74, v69
	v_cvt_i32_f32_e32 v73, v73
	v_exp_f32_e32 v69, v69
	v_cmp_ngt_f32_e64 s[4:5], s68, v68
	v_ldexp_f32 v69, v69, v73
	s_nop 0
	v_cndmask_b32_e64 v69, 0, v69, s[4:5]
	v_cmp_nlt_f32_e64 s[4:5], s69, v68
	s_nop 1
	v_cndmask_b32_e64 v68, v201, v69, s[4:5]
	v_add_f32_e32 v68, 1.0, v68
	v_rcp_f32_e32 v68, v68
	s_nop 0
	v_fma_f32 v73, v68, -2.0, 1.0
.LBB0_717:
	s_andn2_saveexec_b64 s[2:3], s[2:3]
	v_mul_f32_e32 v68, v72, v72
	v_fmamk_f32 v69, v68, 0xbbbac73d, v198
	v_fmaak_f32 v69, v68, v69, 0xbd5c1c4e
	v_fmaak_f32 v69, v68, v69, 0x3e088382
	v_fmaak_f32 v69, v68, v69, 0xbeaaaa99
	v_mul_f32_e64 v69, |v72|, v69
	v_fma_f32 v73, v68, v69, |v72|
	s_or_b64 exec, exec, s[2:3]
	v_sub_u32_e32 v68, s6, v71
	v_add_u32_e32 v68, 0x7e, v68
	v_ashrrev_i32_e32 v69, 31, v68
	v_lshlrev_b64 v[68:69], 6, v[68:69]
	v_lshl_add_u64 v[68:69], s[38:39], 0, v[68:69]
	v_lshl_add_u64 v[68:69], v[68:69], 0, s[40:41]
	global_load_dword v74, v[68:69], off offset:32
	global_load_dword v245, v[68:69], off offset:48
	s_waitcnt vmcnt(0)
	v_mul_f32_e32 v74, 0x3d888889, v74
	v_cmp_nlt_f32_e64 s[2:3], |v74|, s66
	s_and_saveexec_b64 s[4:5], s[2:3]
	s_xor_b64 s[2:3], exec, s[4:5]
	s_cbranch_execz .LBB0_721
	v_add_f32_e64 v75, |v74|, |v74|
	v_mul_f32_e32 v76, 0x3fb8aa3b, v75
	v_rndne_f32_e32 v77, v76
	s_mov_b32 s4, 0x3fb8aa3b
	v_sub_f32_e32 v78, v76, v77
	v_fma_f32 v76, v75, s4, -v76
	v_fmac_f32_e32 v76, 0x32a5705f, v75
	v_add_f32_e32 v76, v78, v76
	v_cvt_i32_f32_e32 v77, v77
	v_exp_f32_e32 v76, v76
	v_cmp_ngt_f32_e64 s[4:5], s68, v75
	v_ldexp_f32 v76, v76, v77
	s_nop 0
	v_cndmask_b32_e64 v76, 0, v76, s[4:5]
	v_cmp_nlt_f32_e64 s[4:5], s69, v75
	s_nop 1
	v_cndmask_b32_e64 v75, v201, v76, s[4:5]
	v_add_f32_e32 v75, 1.0, v75
	v_rcp_f32_e32 v75, v75
	s_nop 0
	v_fma_f32 v75, v75, -2.0, 1.0
.LBB0_721:
	s_andn2_saveexec_b64 s[2:3], s[2:3]
	v_mul_f32_e32 v75, v74, v74
	v_fmamk_f32 v76, v75, 0xbbbac73d, v198
	v_fmaak_f32 v76, v75, v76, 0xbd5c1c4e
	v_fmaak_f32 v76, v75, v76, 0x3e088382
	v_fmaak_f32 v76, v75, v76, 0xbeaaaa99
	v_mul_f32_e64 v76, |v74|, v76
	v_fma_f32 v75, v75, v76, |v74|
	s_or_b64 exec, exec, s[2:3]
	v_mov_b32_e32 v66, v244
	s_waitcnt vmcnt(0)
	v_mul_f32_e32 v76, 0x3d888889, v66
	v_cmp_nlt_f32_e64 s[2:3], |v76|, s66
	s_and_saveexec_b64 s[4:5], s[2:3]
	s_xor_b64 s[2:3], exec, s[4:5]
	s_cbranch_execz .LBB0_725
	v_add_f32_e64 v66, |v76|, |v76|
	v_mul_f32_e32 v67, 0x3fb8aa3b, v66
	v_rndne_f32_e32 v77, v67
	s_mov_b32 s4, 0x3fb8aa3b
	v_sub_f32_e32 v78, v67, v77
	v_fma_f32 v67, v66, s4, -v67
	v_fmac_f32_e32 v67, 0x32a5705f, v66
	v_add_f32_e32 v67, v78, v67
	v_cvt_i32_f32_e32 v77, v77
	v_exp_f32_e32 v67, v67
	v_cmp_ngt_f32_e64 s[4:5], s68, v66
	v_ldexp_f32 v67, v67, v77
	s_nop 0
	v_cndmask_b32_e64 v67, 0, v67, s[4:5]
	v_cmp_nlt_f32_e64 s[4:5], s69, v66
	s_nop 1
	v_cndmask_b32_e64 v66, v201, v67, s[4:5]
	v_add_f32_e32 v66, 1.0, v66
	v_rcp_f32_e32 v66, v66
	s_nop 0
	v_fma_f32 v77, v66, -2.0, 1.0
.LBB0_725:
	s_andn2_saveexec_b64 s[2:3], s[2:3]
	v_mul_f32_e32 v66, v76, v76
	v_fmamk_f32 v67, v66, 0xbbbac73d, v198
	v_fmaak_f32 v67, v66, v67, 0xbd5c1c4e
	v_fmaak_f32 v67, v66, v67, 0x3e088382
	v_fmaak_f32 v67, v66, v67, 0xbeaaaa99
	v_mul_f32_e64 v67, |v76|, v67
	v_fma_f32 v77, v66, v67, |v76|
	s_or_b64 exec, exec, s[2:3]
	v_mov_b32_e32 v66, v245
	s_waitcnt vmcnt(0)
	v_mul_f32_e32 v66, 0x3d888889, v66
	v_cmp_nlt_f32_e64 s[2:3], |v66|, s66
	s_and_saveexec_b64 s[4:5], s[2:3]
	s_xor_b64 s[2:3], exec, s[4:5]
	s_cbranch_execz .LBB0_729
	v_add_f32_e64 v67, |v66|, |v66|
	v_mul_f32_e32 v68, 0x3fb8aa3b, v67
	v_rndne_f32_e32 v69, v68
	s_mov_b32 s4, 0x3fb8aa3b
	v_sub_f32_e32 v78, v68, v69
	v_fma_f32 v68, v67, s4, -v68
	v_fmac_f32_e32 v68, 0x32a5705f, v67
	v_add_f32_e32 v68, v78, v68
	v_cvt_i32_f32_e32 v69, v69
	v_exp_f32_e32 v68, v68
	v_cmp_ngt_f32_e64 s[4:5], s68, v67
	v_ldexp_f32 v68, v68, v69
	s_nop 0
	v_cndmask_b32_e64 v68, 0, v68, s[4:5]
	v_cmp_nlt_f32_e64 s[4:5], s69, v67
	s_nop 1
	v_cndmask_b32_e64 v67, v201, v68, s[4:5]
	v_add_f32_e32 v67, 1.0, v67
	v_rcp_f32_e32 v67, v67
	s_nop 0
	v_fma_f32 v67, v67, -2.0, 1.0

; DI float softcap(float x) { return 15.0f * tanhf(x * (1.0f / 15.0f)); }
; DI float logsigmoid(float y) { return fminf(y, 0.f) - log1pf(__expf(-fabsf(y))); }
; template <bool PASS2, int DIRT>
; DI void mlstm_item(const Params& P, LAS unsigned char* lds, int st, int g) {
;     ...
;     if (wid < nchunks) { const int t0c = chunk_tok0(wid);
;         const int p0 = dir ? 127 - 2 * lane : 2 * lane, p1 = dir ? 126 - 2 * lane : 2 * lane + 1;
;         const float* g0 = gates + (size_t)(t0c + p0) * 16; const float* g1 = gates + (size_t)(t0c + p1) * 16;
;         const float li0 = softcap(g0[dir * 8 + h]), li1 = softcap(g1[dir * 8 + h]); const float lf0 = logsigmoid(softcap(g0[dir * 8 + 4 + h])), lf1 = logsigmoid(softcap(g1[dir * 8 + 4 + h]));
.LBB0_771:
	s_or_b64 exec, exec, s[2:3]
	s_lshr_b32 s1, s42, 6
	s_bfe_u32 s48, s42, 0x20004
	s_cmp_gt_i32 s0, 7
	s_cbranch_scc1 .LBB0_791
	s_lshl_b32 s2, s1, 14
	s_lshl_b32 s3, s96, 10
	v_and_b32_e32 v65, 63, v70
	s_lshl_b32 s4, s0, 7
	s_or_b32 s2, s2, s3
	s_add_i32 s2, s2, s4
	v_lshlrev_b32_e32 v71, 1, v65
	v_or_b32_e32 v68, s2, v71
	v_ashrrev_i32_e32 v69, 31, v68
	v_lshlrev_b64 v[66:67], 6, v[68:69]
	v_lshl_add_u64 v[66:67], s[38:39], 0, v[66:67]
	s_lshl_b32 s40, s48, 2
	v_lshl_add_u64 v[72:73], v[66:67], 0, s[40:41]
	global_load_dword v69, v[72:73], off
	global_load_dword v244, v[72:73], off offset:16
	s_waitcnt vmcnt(0)
	v_mul_f32_e32 v72, 0x3d888889, v69
	v_cmp_nlt_f32_e64 s[2:3], |v72|, s66
	s_and_saveexec_b64 s[4:5], s[2:3]
	s_xor_b64 s[2:3], exec, s[4:5]
	s_cbranch_execz .LBB0_774
	v_add_f32_e64 v69, |v72|, |v72|
	v_mul_f32_e32 v73, 0x3fb8aa3b, v69
	v_rndne_f32_e32 v74, v73
	s_mov_b32 s4, 0x3fb8aa3b
	v_sub_f32_e32 v75, v73, v74
	v_fma_f32 v73, v69, s4, -v73
	v_fmac_f32_e32 v73, 0x32a5705f, v69
	v_add_f32_e32 v73, v75, v73
	v_cvt_i32_f32_e32 v74, v74
	v_exp_f32_e32 v73, v73
	v_cmp_ngt_f32_e64 s[4:5], s68, v69
	v_ldexp_f32 v73, v73, v74
	s_nop 0
	v_cndmask_b32_e64 v73, 0, v73, s[4:5]
	v_cmp_nlt_f32_e64 s[4:5], s69, v69
	s_nop 1
	v_cndmask_b32_e64 v69, v201, v73, s[4:5]
	v_add_f32_e32 v69, 1.0, v69
	v_rcp_f32_e32 v69, v69
	s_nop 0
	v_fma_f32 v73, v69, -2.0, 1.0
.LBB0_774:
	s_andn2_saveexec_b64 s[2:3], s[2:3]
	v_mul_f32_e32 v69, v72, v72
	v_fmamk_f32 v73, v69, 0xbbbac73d, v198
	v_fmaak_f32 v73, v69, v73, 0xbd5c1c4e
	v_fmaak_f32 v73, v69, v73, 0x3e088382
	v_fmaak_f32 v73, v69, v73, 0xbeaaaa99
	v_mul_f32_e64 v73, |v72|, v73
	v_fma_f32 v73, v69, v73, |v72|
	s_or_b64 exec, exec, s[2:3]
	v_or_b32_e32 v68, 1, v68
	v_ashrrev_i32_e32 v69, 31, v68
	v_lshlrev_b64 v[68:69], 6, v[68:69]
	v_lshl_add_u64 v[68:69], s[38:39], 0, v[68:69]
	v_lshl_add_u64 v[74:75], v[68:69], 0, s[40:41]
	global_load_dword v74, v[74:75], off
	global_load_dword v245, v[74:75], off offset:16
	s_waitcnt vmcnt(0)
	v_mul_f32_e32 v74, 0x3d888889, v74
	v_cmp_nlt_f32_e64 s[2:3], |v74|, s66
	s_and_saveexec_b64 s[4:5], s[2:3]
	s_xor_b64 s[2:3], exec, s[4:5]
	s_cbranch_execz .LBB0_778
	v_add_f32_e64 v75, |v74|, |v74|
	v_mul_f32_e32 v76, 0x3fb8aa3b, v75
	v_rndne_f32_e32 v77, v76
	s_mov_b32 s4, 0x3fb8aa3b
	v_sub_f32_e32 v78, v76, v77
	v_fma_f32 v76, v75, s4, -v76
	v_fmac_f32_e32 v76, 0x32a5705f, v75
	v_add_f32_e32 v76, v78, v76
	v_cvt_i32_f32_e32 v77, v77
	v_exp_f32_e32 v76, v76
	v_cmp_ngt_f32_e64 s[4:5], s68, v75
	v_ldexp_f32 v76, v76, v77
	s_nop 0
	v_cndmask_b32_e64 v76, 0, v76, s[4:5]
	v_cmp_nlt_f32_e64 s[4:5], s69, v75
	s_nop 1
	v_cndmask_b32_e64 v75, v201, v76, s[4:5]
	v_add_f32_e32 v75, 1.0, v75
	v_rcp_f32_e32 v75, v75
	s_nop 0
	v_fma_f32 v75, v75, -2.0, 1.0
.LBB0_778:
	s_andn2_saveexec_b64 s[2:3], s[2:3]
	v_mul_f32_e32 v75, v74, v74
	v_fmamk_f32 v76, v75, 0xbbbac73d, v198
	v_fmaak_f32 v76, v75, v76, 0xbd5c1c4e
	v_fmaak_f32 v76, v75, v76, 0x3e088382
	v_fmaak_f32 v76, v75, v76, 0xbeaaaa99
	v_mul_f32_e64 v76, |v74|, v76
	v_fma_f32 v75, v75, v76, |v74|
	s_or_b64 exec, exec, s[2:3]
	s_lshr_b32 s2, s42, 4
	s_or_b32 s2, s2, 4
	s_lshl_b32 s40, s2, 2
	v_lshl_add_u64 v[66:67], v[66:67], 0, s[40:41]
	v_mov_b32_e32 v66, v244
	s_waitcnt vmcnt(0)
	v_mul_f32_e32 v76, 0x3d888889, v66
	v_cmp_nlt_f32_e64 s[2:3], |v76|, s66
	s_and_saveexec_b64 s[4:5], s[2:3]
	s_xor_b64 s[2:3], exec, s[4:5]
	s_cbranch_execz .LBB0_782
	v_add_f32_e64 v66, |v76|, |v76|
	v_mul_f32_e32 v67, 0x3fb8aa3b, v66
	v_rndne_f32_e32 v77, v67
	s_mov_b32 s4, 0x3fb8aa3b
	v_sub_f32_e32 v78, v67, v77
	v_fma_f32 v67, v66, s4, -v67
	v_fmac_f32_e32 v67, 0x32a5705f, v66
	v_add_f32_e32 v67, v78, v67
	v_cvt_i32_f32_e32 v77, v77
	v_exp_f32_e32 v67, v67
	v_cmp_ngt_f32_e64 s[4:5], s68, v66
	v_ldexp_f32 v67, v67, v77
	s_nop 0
	v_cndmask_b32_e64 v67, 0, v67, s[4:5]
	v_cmp_nlt_f32_e64 s[4:5], s69, v66
	s_nop 1
	v_cndmask_b32_e64 v66, v201, v67, s[4:5]
	v_add_f32_e32 v66, 1.0, v66
	v_rcp_f32_e32 v66, v66
	s_nop 0
	v_fma_f32 v77, v66, -2.0, 1.0
.LBB0_782:
	s_andn2_saveexec_b64 s[2:3], s[2:3]
	v_mul_f32_e32 v66, v76, v76
	v_fmamk_f32 v67, v66, 0xbbbac73d, v198
	v_fmaak_f32 v67, v66, v67, 0xbd5c1c4e
	v_fmaak_f32 v67, v66, v67, 0x3e088382
	v_fmaak_f32 v67, v66, v67, 0xbeaaaa99
	v_mul_f32_e64 v67, |v76|, v67
	v_fma_f32 v77, v66, v67, |v76|
	s_or_b64 exec, exec, s[2:3]
	v_lshl_add_u64 v[66:67], v[68:69], 0, s[40:41]
	v_mov_b32_e32 v66, v245
	s_waitcnt vmcnt(0)
	v_mul_f32_e32 v66, 0x3d888889, v66
	v_cmp_nlt_f32_e64 s[2:3], |v66|, s66
	s_and_saveexec_b64 s[4:5], s[2:3]
	s_xor_b64 s[2:3], exec, s[4:5]
	s_cbranch_execz .LBB0_786
	v_add_f32_e64 v67, |v66|, |v66|
	v_mul_f32_e32 v68, 0x3fb8aa3b, v67
	v_rndne_f32_e32 v69, v68
	s_mov_b32 s4, 0x3fb8aa3b
	v_sub_f32_e32 v78, v68, v69
	v_fma_f32 v68, v67, s4, -v68
	v_fmac_f32_e32 v68, 0x32a5705f, v67
	v_add_f32_e32 v68, v78, v68
	v_cvt_i32_f32_e32 v69, v69
	v_exp_f32_e32 v68, v68
	v_cmp_ngt_f32_e64 s[4:5], s68, v67
	v_ldexp_f32 v68, v68, v69
	s_nop 0
	v_cndmask_b32_e64 v68, 0, v68, s[4:5]
	v_cmp_nlt_f32_e64 s[4:5], s69, v67
	s_nop 1
	v_cndmask_b32_e64 v67, v201, v68, s[4:5]
	v_add_f32_e32 v67, 1.0, v67
	v_rcp_f32_e32 v67, v67
	s_nop 0
	v_fma_f32 v67, v67, -2.0, 1.0
